# speedup vs baseline: 1.0007x; 1.0007x over previous
.LBB4_52:
	v_add_u32_e32 v1, s8, v42
	ds_read_b128 v[2:5], v0
	ds_read_b128 v[6:9], v0 offset:16
	v_add_u32_e32 v12, s8, v41
	ds_read2_b32 v[10:11], v1 offset1:100
	ds_read2_b32 v[24:25], v12 offset1:100
	v_add_u32_e32 v13, 0x200, v1
	v_add_u32_e32 v14, 0x200, v12
	v_add_u32_e32 v15, 0x400, v1
	v_add_u32_e32 v16, 0x400, v12
	v_add_u32_e32 v1, 0x800, v1
	v_add_u32_e32 v18, 0x800, v12
	ds_read2_b32 v[12:13], v13 offset0:72 offset1:172
	ds_read2_b32 v[26:27], v14 offset0:72 offset1:172
	ds_read2_b32 v[14:15], v15 offset0:144 offset1:244
	ds_read2_b32 v[28:29], v16 offset0:144 offset1:244
	ds_read2_b32 v[16:17], v1 offset0:88 offset1:188
	ds_read2_b32 v[30:31], v18 offset0:88 offset1:188
	s_waitcnt lgkmcnt(6)
	v_fmac_f32_e32 v39, v2, v10
	v_fmac_f32_e32 v38, v2, v24
	v_fmac_f32_e32 v39, v3, v11
	v_fmac_f32_e32 v38, v3, v25
	s_waitcnt lgkmcnt(4)
	v_fmac_f32_e32 v39, v4, v12
	v_fmac_f32_e32 v38, v4, v26
	v_fmac_f32_e32 v39, v5, v13
	v_fmac_f32_e32 v38, v5, v27
	s_waitcnt lgkmcnt(2)
	v_fmac_f32_e32 v39, v6, v14
	v_fmac_f32_e32 v38, v6, v28
	v_fmac_f32_e32 v39, v7, v15
	v_fmac_f32_e32 v38, v7, v29
	s_waitcnt lgkmcnt(0)
	v_fmac_f32_e32 v39, v8, v16
	v_fmac_f32_e32 v38, v8, v30
	v_fmac_f32_e32 v39, v9, v17
	v_fmac_f32_e32 v38, v9, v31
	s_addk_i32 s8, 0xc80
	v_add_u32_e32 v0, 32, v0
	s_cmpk_eq_i32 s8, 0x6400
	s_cbranch_scc0 .LBB4_52
	v_cmp_nlt_f32_e64 s[0:1], 0, v39
	s_and_saveexec_b64 s[2:3], s[0:1]
	s_cbranch_execz .LBB4_55
	v_mul_f32_e32 v0, 0x3fb8aa3b, v39
	v_rndne_f32_e32 v0, v0
	v_fmamk_f32 v1, v0, 0xbf317218, v39
	v_fmamk_f32 v1, v0, 0x3102e308, v1
	v_mov_b32_e32 v2, 0x3ab69700
	v_fmac_f32_e32 v2, 0x395133b1, v1
	v_fmaak_f32 v2, v1, v2, 0x3c0887f9
	v_fmaak_f32 v2, v1, v2, 0x3d2aaa81
	v_cvt_i32_f32_e32 v3, v0
	v_fmaak_f32 v2, v1, v2, 0x3e2aaaab
	v_fma_f32 v2, v1, v2, 0.5
	v_mul_f32_e32 v2, v1, v2
	s_mov_b32 s0, 0x43000000
	v_fmac_f32_e32 v1, v1, v2
	v_ldexp_f32 v2, 1.0, v3
	v_mov_b32_e32 v3, 0x7f000000
	v_cmp_eq_f32_e64 s[0:1], s0, v0
	s_nop 1
	v_cndmask_b32_e64 v0, v2, v3, s[0:1]
	v_add_f32_e32 v2, -1.0, v0
	v_fmac_f32_e32 v2, v0, v1
	v_add_f32_e32 v0, v2, v2
	v_cndmask_b32_e64 v0, v2, v0, s[0:1]
	s_mov_b32 s0, 0xc1880000
	v_cmp_ngt_f32_e64 s[0:1], s0, v39
	s_nop 1
	v_cndmask_b32_e64 v39, -1.0, v0, s[0:1]
